# ssd pass3 norm epilogue loads batched with counted vmcnt and prologue X copy loads pipelined, on top of v13
# speedup vs baseline: 1.1067x; 1.0005x over previous
.LBB0_154:
	s_mov_b64 s[0:1], 0x820000
	v_cmp_gt_i64_e32 vcc, s[0:1], v[2:3]
	s_barrier
	s_and_saveexec_b64 s[0:1], vcc
	s_cbranch_execz .LBB0_157
	s_ashr_i32 s3, s2, 31
	s_lshl_b64 s[6:7], s[2:3], 9
	s_add_u32 s8, s8, 0xf8000000
	s_addc_u32 s9, s9, -1
	s_lshl_b64 s[10:11], s[36:37], 13
	v_lshl_add_u64 v[4:5], v[8:9], 4, s[10:11]
	s_lshl_b64 s[10:11], s[2:3], 13
	s_lshl_b64 s[12:13], s[36:37], 12
	s_add_u32 s12, s34, s12
	s_addc_u32 s13, s35, s13
	v_lshl_add_u64 v[6:7], v[8:9], 3, s[12:13]
	s_mov_b64 s[12:13], 0xe5f0000
	v_lshl_add_u64 v[6:7], v[6:7], 0, s[12:13]
	s_lshl_b64 s[12:13], s[2:3], 12
	s_mov_b64 s[14:15], 0
	s_mov_b64 s[16:17], 0x800000
	s_mov_b64 s[18:19], 0x81ffff
	s_mov_b64 s[14:15], exec
.LBB0_156:
	v_cmp_ge_i64_e64 s[20:21], s[18:19], v[2:3]
	v_cmp_gt_i64_e32 vcc, s[16:17], v[2:3]
	v_lshl_add_u64 v[8:9], s[4:5], 0, v[4:5]
	v_lshl_add_u64 v[10:11], s[8:9], 0, v[4:5]
	v_cndmask_b32_e32 v13, v11, v9, vcc
	v_cndmask_b32_e32 v12, v10, v8, vcc
	s_and_b64 exec, s[14:15], s[20:21]
	global_load_dwordx4 v[16:19], v[12:13], off
	s_mov_b64 exec, s[14:15]
	v_lshl_add_u64 v[2:3], v[2:3], 0, s[6:7]
	v_lshl_add_u64 v[4:5], v[4:5], 0, s[10:11]
	v_cmp_ge_i64_e64 s[22:23], s[18:19], v[2:3]
	v_cmp_gt_i64_e32 vcc, s[16:17], v[2:3]
	v_lshl_add_u64 v[8:9], s[4:5], 0, v[4:5]
	v_lshl_add_u64 v[10:11], s[8:9], 0, v[4:5]
	v_cndmask_b32_e32 v13, v11, v9, vcc
	v_cndmask_b32_e32 v12, v10, v8, vcc
	s_and_b64 exec, s[14:15], s[22:23]
	global_load_dwordx4 v[20:23], v[12:13], off
	s_mov_b64 exec, s[14:15]
	v_lshl_add_u64 v[2:3], v[2:3], 0, s[6:7]
	v_lshl_add_u64 v[4:5], v[4:5], 0, s[10:11]
	v_cmp_ge_i64_e64 s[24:25], s[18:19], v[2:3]
	v_cmp_gt_i64_e32 vcc, s[16:17], v[2:3]
	v_lshl_add_u64 v[8:9], s[4:5], 0, v[4:5]
	v_lshl_add_u64 v[10:11], s[8:9], 0, v[4:5]
	v_cndmask_b32_e32 v13, v11, v9, vcc
	v_cndmask_b32_e32 v12, v10, v8, vcc
	s_and_b64 exec, s[14:15], s[24:25]
	global_load_dwordx4 v[24:27], v[12:13], off
	s_mov_b64 exec, s[14:15]
	v_lshl_add_u64 v[2:3], v[2:3], 0, s[6:7]
	v_lshl_add_u64 v[4:5], v[4:5], 0, s[10:11]
	s_waitcnt vmcnt(0)
	s_and_b64 exec, s[14:15], s[20:21]
	v_cvt_pk_bf16_f32 v16, v16, v17
	v_cvt_pk_bf16_f32 v17, v18, v19
	global_store_dwordx2 v[6:7], v[16:17], off
	s_mov_b64 exec, s[14:15]
	v_lshl_add_u64 v[6:7], v[6:7], 0, s[12:13]
	s_and_b64 exec, s[14:15], s[22:23]
	v_cvt_pk_bf16_f32 v20, v20, v21
	v_cvt_pk_bf16_f32 v21, v22, v23
	global_store_dwordx2 v[6:7], v[20:21], off
	s_mov_b64 exec, s[14:15]
	v_lshl_add_u64 v[6:7], v[6:7], 0, s[12:13]
	s_and_b64 exec, s[14:15], s[24:25]
	v_cvt_pk_bf16_f32 v24, v24, v25
	v_cvt_pk_bf16_f32 v25, v26, v27
	global_store_dwordx2 v[6:7], v[24:25], off
	s_mov_b64 exec, s[14:15]
	v_lshl_add_u64 v[6:7], v[6:7], 0, s[12:13]
	v_cmp_ge_i64_e32 vcc, s[18:19], v[2:3]
	s_cbranch_vccnz .LBB0_156

.LBB0_1408:
	s_nop 1
	v_lshl_add_u64 v[8:9], s[8:9], 0, v[2:3]
	v_add_co_u32_e32 v24, vcc, 0x3c134000, v8
	v_lshl_add_u64 v[20:21], v[6:7], 0, s[0:1]
	s_nop 0
	v_addc_co_u32_e32 v25, vcc, 0, v9, vcc
	global_load_dwordx4 v[26:29], v[24:25], off offset:256
	global_load_dwordx4 v[30:33], v[24:25], off offset:320
	global_load_dwordx4 v[34:37], v[24:25], off offset:384
	global_load_dwordx4 v[38:41], v[24:25], off offset:448
	global_load_dwordx4 v[42:45], v[24:25], off offset:512
	global_load_dwordx4 v[46:49], v[24:25], off offset:576
	global_load_dwordx4 v[50:53], v[24:25], off offset:640
	global_load_dwordx4 v[54:57], v[24:25], off offset:704
	global_load_dwordx4 v[58:61], v[24:25], off offset:768
	global_load_dwordx4 v[62:65], v[24:25], off offset:832
	global_load_dwordx4 v[66:69], v[24:25], off offset:896
	global_load_dwordx4 v[70:73], v[24:25], off offset:960
	global_load_dwordx4 v[74:77], v[20:21], off
	global_load_dwordx4 v[78:81], v[20:21], off offset:64
	global_load_dwordx4 v[84:87], v[20:21], off offset:128
	global_load_dwordx4 v[88:91], v[20:21], off offset:192
	global_load_dwordx4 v[92:95], v[20:21], off offset:256
	global_load_dwordx4 v[96:99], v[20:21], off offset:320
	global_load_dwordx4 v[100:103], v[20:21], off offset:384
	global_load_dwordx4 v[104:107], v[20:21], off offset:448
	global_load_dwordx4 v[108:111], v[20:21], off offset:512
	global_load_dwordx4 v[112:115], v[20:21], off offset:576
	global_load_dwordx4 v[118:121], v[20:21], off offset:640
	global_load_dwordx4 v[122:125], v[20:21], off offset:704
	v_lshl_add_u64 v[22:23], s[8:9], 0, v[4:5]
	v_add_co_u32_e32 v8, vcc, s4, v22
	s_add_u32 s0, s0, 0x300
	s_nop 0
	v_addc_co_u32_e32 v9, vcc, 0, v23, vcc
	s_mov_b64 s[2:3], 0x300
	s_addc_u32 s1, s1, 0
	v_lshl_add_u64 v[4:5], v[4:5], 0, s[6:7]
	v_lshl_add_u64 v[2:3], v[2:3], 0, s[2:3]
	s_cmpk_lg_i32 s0, 0x600
	s_waitcnt vmcnt(11)
	v_mul_f32_e32 v26, v10, v26
	v_mul_f32_e32 v27, v10, v27
	v_mul_f32_e32 v28, v10, v28
	v_mul_f32_e32 v29, v10, v29
	v_mul_f32_e32 v26, v74, v26
	v_mul_f32_e32 v27, v75, v27
	v_mul_f32_e32 v28, v76, v28
	v_mul_f32_e32 v29, v77, v29
	v_cvt_pk_bf16_f32 v26, v26, v27
	v_cvt_pk_bf16_f32 v27, v28, v29
	global_store_dwordx2 v[8:9], v[26:27], off
	s_waitcnt vmcnt(11)
	v_mul_f32_e32 v30, v10, v30
	v_mul_f32_e32 v31, v10, v31
	v_mul_f32_e32 v32, v10, v32
	v_mul_f32_e32 v33, v10, v33
	v_mul_f32_e32 v30, v78, v30
	v_mul_f32_e32 v31, v79, v31
	v_mul_f32_e32 v32, v80, v32
	v_mul_f32_e32 v33, v81, v33
	v_cvt_pk_bf16_f32 v30, v30, v31
	v_cvt_pk_bf16_f32 v31, v32, v33
	global_store_dwordx2 v[8:9], v[30:31], off offset:32
	s_waitcnt vmcnt(11)
	v_mul_f32_e32 v34, v10, v34
	v_mul_f32_e32 v35, v10, v35
	v_mul_f32_e32 v36, v10, v36
	v_mul_f32_e32 v37, v10, v37
	v_mul_f32_e32 v34, v84, v34
	v_mul_f32_e32 v35, v85, v35
	v_mul_f32_e32 v36, v86, v36
	v_mul_f32_e32 v37, v87, v37
	v_cvt_pk_bf16_f32 v34, v34, v35
	v_cvt_pk_bf16_f32 v35, v36, v37
	global_store_dwordx2 v[8:9], v[34:35], off offset:64
	s_waitcnt vmcnt(11)
	v_mul_f32_e32 v38, v10, v38
	v_mul_f32_e32 v39, v10, v39
	v_mul_f32_e32 v40, v10, v40
	v_mul_f32_e32 v41, v10, v41
	v_mul_f32_e32 v38, v88, v38
	v_mul_f32_e32 v39, v89, v39
	v_mul_f32_e32 v40, v90, v40
	v_mul_f32_e32 v41, v91, v41
	v_cvt_pk_bf16_f32 v38, v38, v39
	v_cvt_pk_bf16_f32 v39, v40, v41
	global_store_dwordx2 v[8:9], v[38:39], off offset:96
	s_waitcnt vmcnt(11)
	v_mul_f32_e32 v42, v10, v42
	v_mul_f32_e32 v43, v10, v43
	v_mul_f32_e32 v44, v10, v44
	v_mul_f32_e32 v45, v10, v45
	v_mul_f32_e32 v42, v92, v42
	v_mul_f32_e32 v43, v93, v43
	v_mul_f32_e32 v44, v94, v44
	v_mul_f32_e32 v45, v95, v45
	v_cvt_pk_bf16_f32 v42, v42, v43
	v_cvt_pk_bf16_f32 v43, v44, v45
	global_store_dwordx2 v[8:9], v[42:43], off offset:128
	s_waitcnt vmcnt(11)
	v_mul_f32_e32 v46, v10, v46
	v_mul_f32_e32 v47, v10, v47
	v_mul_f32_e32 v48, v10, v48
	v_mul_f32_e32 v49, v10, v49
	v_mul_f32_e32 v46, v96, v46
	v_mul_f32_e32 v47, v97, v47
	v_mul_f32_e32 v48, v98, v48
	v_mul_f32_e32 v49, v99, v49
	v_cvt_pk_bf16_f32 v46, v46, v47
	v_cvt_pk_bf16_f32 v47, v48, v49
	global_store_dwordx2 v[8:9], v[46:47], off offset:160
	s_waitcnt vmcnt(11)
	v_mul_f32_e32 v50, v10, v50
	v_mul_f32_e32 v51, v10, v51
	v_mul_f32_e32 v52, v10, v52
	v_mul_f32_e32 v53, v10, v53
	v_mul_f32_e32 v50, v100, v50
	v_mul_f32_e32 v51, v101, v51
	v_mul_f32_e32 v52, v102, v52
	v_mul_f32_e32 v53, v103, v53
	v_cvt_pk_bf16_f32 v50, v50, v51
	v_cvt_pk_bf16_f32 v51, v52, v53
	global_store_dwordx2 v[8:9], v[50:51], off offset:192
	s_waitcnt vmcnt(11)
	v_mul_f32_e32 v54, v10, v54
	v_mul_f32_e32 v55, v10, v55
	v_mul_f32_e32 v56, v10, v56
	v_mul_f32_e32 v57, v10, v57
	v_mul_f32_e32 v54, v104, v54
	v_mul_f32_e32 v55, v105, v55
	v_mul_f32_e32 v56, v106, v56
	v_mul_f32_e32 v57, v107, v57
	v_cvt_pk_bf16_f32 v54, v54, v55
	v_cvt_pk_bf16_f32 v55, v56, v57
	global_store_dwordx2 v[8:9], v[54:55], off offset:224
	s_waitcnt vmcnt(11)
	v_mul_f32_e32 v58, v10, v58
	v_mul_f32_e32 v59, v10, v59
	v_mul_f32_e32 v60, v10, v60
	v_mul_f32_e32 v61, v10, v61
	v_mul_f32_e32 v58, v108, v58
	v_mul_f32_e32 v59, v109, v59
	v_mul_f32_e32 v60, v110, v60
	v_mul_f32_e32 v61, v111, v61
	v_cvt_pk_bf16_f32 v58, v58, v59
	v_cvt_pk_bf16_f32 v59, v60, v61
	global_store_dwordx2 v[8:9], v[58:59], off offset:256
	s_waitcnt vmcnt(11)
	v_mul_f32_e32 v62, v10, v62
	v_mul_f32_e32 v63, v10, v63
	v_mul_f32_e32 v64, v10, v64
	v_mul_f32_e32 v65, v10, v65
	v_mul_f32_e32 v62, v112, v62
	v_mul_f32_e32 v63, v113, v63
	v_mul_f32_e32 v64, v114, v64
	v_mul_f32_e32 v65, v115, v65
	v_cvt_pk_bf16_f32 v62, v62, v63
	v_cvt_pk_bf16_f32 v63, v64, v65
	global_store_dwordx2 v[8:9], v[62:63], off offset:288
	s_waitcnt vmcnt(11)
	v_mul_f32_e32 v66, v10, v66
	v_mul_f32_e32 v67, v10, v67
	v_mul_f32_e32 v68, v10, v68
	v_mul_f32_e32 v69, v10, v69
	v_mul_f32_e32 v66, v118, v66
	v_mul_f32_e32 v67, v119, v67
	v_mul_f32_e32 v68, v120, v68
	v_mul_f32_e32 v69, v121, v69
	v_cvt_pk_bf16_f32 v66, v66, v67
	v_cvt_pk_bf16_f32 v67, v68, v69
	global_store_dwordx2 v[8:9], v[66:67], off offset:320
	s_waitcnt vmcnt(11)
	v_mul_f32_e32 v70, v10, v70
	v_mul_f32_e32 v71, v10, v71
	v_mul_f32_e32 v72, v10, v72
	v_mul_f32_e32 v73, v10, v73
	v_mul_f32_e32 v70, v122, v70
	v_mul_f32_e32 v71, v123, v71
	v_mul_f32_e32 v72, v124, v72
	v_mul_f32_e32 v73, v125, v73
	v_cvt_pk_bf16_f32 v70, v70, v71
	v_cvt_pk_bf16_f32 v71, v72, v73
	global_store_dwordx2 v[8:9], v[70:71], off offset:352
	s_cbranch_scc1 .LBB0_1408
	v_mov_b32_e32 v2, v0
	s_mov_b32 s80, 0x25bb0000
	s_barrier
	s_nop 0
	v_cmp_eq_u32_e32 vcc, 0, v2
	s_and_saveexec_b64 s[0:1], vcc
	s_cbranch_execz .LBB0_917
	v_readlane_b32 s4, v252, 14
	s_mov_b64 s[2:3], exec
	s_nop 0
	v_mov_b32_e32 v2, s4
	ds_write_b32 v2, v154
	v_mbcnt_lo_u32_b32 v2, s2, 0
	v_mbcnt_hi_u32_b32 v2, s3, v2
	v_cmp_eq_u32_e32 vcc, 0, v2
	s_and_saveexec_b64 s[4:5], vcc
	s_cbranch_execz .LBB0_916
	s_bcnt1_i32_b64 s2, s[2:3]
	v_mov_b32_e32 v3, s2
	v_readlane_b32 s2, v253, 19
	v_readlane_b32 s3, v253, 20
	s_nop 4
	global_atomic_add v3, v83, v3, s[2:3] sc0
	s_branch .LBB0_916
